# same as the three-epilogue version with a 4-byte pad ahead of the expert GEMM loops so they start 8-byte aligned again (code placement)
# baseline (speedup 1.0000x reference)
;     __device__ __forceinline__ bool next(int i, Unit& u) const { if (!order_tile(i, G, c, nM, nN, u.pm, u.pn)) return false; u.A = A0 + (size_t)u.pm * tstep; u.B = B0 + (size_t)u.pn * tstep; return true; }
;     __device__ __forceinline__ bool next(int i, Unit& u) const { if (!order_tile(i, G, c, nM, nN, u.pm, u.pn)) return false; u.A = A0 + (size_t)(u.pn >> 1) * groupA + (size_t)u.pm * tstep; u.B = B0 + (size_t)u.pn * tstep; return true; }
; #define PG8_STAGE(bufoff, gbase, voff) do { _Pragma("unroll") for (int _i = 0; _i < 2; ++_i) glds16_s((const void*)((const char*)(gbase) + _i * r64), (voff), ldsb + (unsigned)(bufoff) + ldsw + _i * 8192u); } while (0)
; #define PG8_WAIT_V(n) asm volatile("s_waitcnt vmcnt(" #n ")" ::: "memory")
; #define PG8_BAR __builtin_amdgcn_s_barrier()
; template <class Epi, class Sched, bool FP8 = false>
; __device__ __forceinline__ void gemm_phase(LAS unsigned char* lds, const int Kb, const int nt  , const Sched& S, const Epi& E) {
;     ...
;     { int R, C; stage_rc(tid * 16, R, C); const int Rb = Epi::PERM ? ((R & ~31) + perm32(R & 31)) : R;
;         voffA = (unsigned)(R * Kb + C * 2); voffB = (unsigned)(Rb * Kb + C * 2); }
;     const size_t r64 = (size_t)64 * Kb;
;     const size_t kstep = (size_t)(BK * 2);
;     const size_t hstep = (size_t)HALF * Kb;
;     const unsigned ldsw = (unsigned)wid * 1024u, ldsb = (unsigned)(uintptr_t)lds;
;     const int aoff = lds_byte(wr * 64 + fr, fq * 8), boff = lds_byte(wc * 32 + fr, fq * 8);
;     ...
;     Unit cur, nxt; int ui = 0;
;     if (!S.next(0, cur)) return;
;     f32x4 acc[2][2][4][2];
; #pragma unroll
;     for (int a = 0; a < 2; ++a)
; #pragma unroll
;         for (int b = 0; b < 2; ++b)
; #pragma unroll
;             for (int m = 0; m < 4; ++m)
; #pragma unroll
;                 for (int n = 0; n < 2; ++n) acc[a][b][m][n] = (f32x4){0.f, 0.f, 0.f, 0.f};
;     bf16x8 At[4][2], B0[2][2], B1[2][2]; i32x8 A8[4], B08[2], B18[2];
;     const char* cA = cur.A; const char* cB = cur.B;
;     PG8_STAGE(PG8_SB(0, 0), cB, voffB); PG8_STAGE(PG8_SA(0, 0), cA, voffA); PG8_STAGE(PG8_SB(0, 1), cB + hstep, voffB); PG8_STAGE(PG8_SA(0, 1), cA + hstep, voffA);
;     if (wr == 1) PG8_BAR;
;     PG8_WAIT_V(4); PG8_BAR;
;     PG8_STAGE(PG8_SB(1, 0), cB + kstep, voffB); PG8_STAGE(PG8_SA(1, 0), cA + kstep, voffA); PG8_STAGE(PG8_SB(1, 1), cB + hstep + kstep, voffB);
;     PG8_WAIT_V(6); PG8_BAR;
.LBB0_2748:
	v_readlane_b32 s2, v241, 5
	v_readlane_b32 s3, v241, 6
	s_add_u32 s2, s2, 0x31500000
	s_addc_u32 s3, s3, 0
	s_lshl_b32 s6, s6, 5
	s_and_b32 s55, s6, 0x60
	s_lshl_b32 s54, s7, 6
	s_lshl_b32 s8, s7, 13
	s_lshl_b32 s9, s55, 7
	s_add_u32 s6, s24, 0x80
	s_addc_u32 s7, s25, 0
	s_add_i32 s57, s19, 0x18000
	s_waitcnt vmcnt(4)
	s_barrier
	s_mov_b32 s10, m0
	s_mov_b32 m0, s57
	s_nop 0
	global_load_lds_dwordx4 v138, s[6:7]
	s_mov_b32 m0, s10
	s_add_u32 s6, s24, 0x20080
	s_addc_u32 s7, s25, 0
	s_add_i32 s58, s19, 0x1a000
	s_mov_b32 s10, m0
	s_mov_b32 m0, s58
	s_nop 0
	global_load_lds_dwordx4 v138, s[6:7]
	s_mov_b32 m0, s10
	s_add_u32 s6, s22, 0x80
	s_addc_u32 s7, s23, 0
	s_add_i32 s59, s19, 0x8000
	s_mov_b32 s10, m0
	s_mov_b32 m0, s59
	s_nop 0
	global_load_lds_dwordx4 v1, s[6:7]
	s_mov_b32 m0, s10
	s_add_u32 s6, s22, 0x20080
	s_addc_u32 s7, s23, 0
	s_add_i32 s60, s19, 0xa000
	s_mov_b32 s10, m0
	s_mov_b32 m0, s60
	s_nop 0
	global_load_lds_dwordx4 v1, s[6:7]
	s_mov_b32 m0, s10
	s_add_u32 s6, s24, 0x40080
	s_addc_u32 s7, s25, 0
	s_add_i32 s61, s19, 0x1c000
	v_lshlrev_b32_e32 v3, 6, v0
	v_lshlrev_b32_e32 v4, 2, v0
	s_mov_b32 s10, m0
	s_mov_b32 m0, s61
	s_nop 0
	global_load_lds_dwordx4 v138, s[6:7]
	s_mov_b32 m0, s10
	s_add_u32 s6, s24, 0x60080
	v_and_b32_e32 v2, 48, v0
	v_and_b32_e32 v3, 0x3c0, v3
	v_and_b32_e32 v4, 32, v4
	s_addc_u32 s7, s25, 0
	s_add_i32 s62, s19, 0x1e000
	s_mov_b32 s10, m0
	s_mov_b32 m0, s62
	s_nop 0
	global_load_lds_dwordx4 v138, s[6:7]
	s_mov_b32 m0, s10
	v_bitop3_b32 v2, v3, v4, v2 bitop3:0x36
	s_waitcnt vmcnt(6)
	s_add_i32 s6, s9, 0
	v_add_u32_e32 v3, s6, v2
	v_add_u32_e32 v2, 0, v2
	s_mov_b32 s6, 0x39000000
	s_mov_b32 s56, 0
	s_add_i32 s63, s19, 0xc000
	v_add_u32_e32 v139, 0x10000, v3
	v_add_u32_e32 v140, 0x10400, v3
	v_add_u32_e32 v141, 0x10800, v3
	v_add_u32_e32 v142, 0x10c00, v3
	s_add_i32 s64, s19, 0xe000
	v_add_u32_e32 v143, 0x14000, v3
	v_add_u32_e32 v144, 0x14400, v3
	v_add_u32_e32 v145, 0x14800, v3
	v_add_u32_e32 v146, 0x14c00, v3
	v_add_u32_e32 v147, 0x18000, v3
	v_add_u32_e32 v148, 0x18400, v3
	v_add_u32_e32 v149, 0x18800, v3
	v_add_u32_e32 v150, 0x18c00, v3
	v_add_u32_e32 v151, 0x1c000, v3
	v_add_u32_e32 v152, 0x1c400, v3
	v_add_u32_e32 v153, 0x1c800, v3
	v_add_u32_e32 v154, 0x1cc00, v3
	v_add_u32_e32 v155, s8, v2
	v_mov_b32_e32 v156, 0x7f7f7f7f
	s_movk_i32 s65, 0x1c00
	s_mov_b32 s7, 0x3a800000
	s_mov_b32 s66, 0xc3e00000
	v_mov_b32_e32 v157, 0x43e00000
	s_mov_b64 s[16:17], s[24:25]
	s_mov_b64 s[14:15], s[22:23]
	s_barrier
	s_nop 0
